# v030 + CSW table loads hoisted (56+8 in flight) + routed-down epilogue with row-table reads up front and bpermutes pipelined one group ahead of the stores
# speedup vs baseline: 1.0173x; 1.0037x over previous
; __device__ __forceinline__ void phase_p0a(const Ptrs& P, LAS unsigned char* lds, int tid_, int vcu, int G) {
;     ...
;     for (size_t i = gt; i < (size_t)NL * 2 * 4 * 64 * 64; i += NGT) { const int e = (int)(i & 63), d = (int)((i >> 6) & 63), h = (int)((i >> 12) & 3), kind = (int)((i >> 14) & 1), l = (int)(i >> 15);
;         const float* fw = P.four_w + ((size_t)(l * 4 + h) * 64) * 64 + e; float s = 0.f;
; #pragma unroll 8
;         for (int kp = 0; kp < 64; ++kp) s += t64[kind * 64 + ((kp * d) & 63)] * fw[kp * 64];
;         ((float*)(P.ws + WS_CSW))[i] = s * 0.00276213586f; }
.LBB0_103:
	s_waitcnt vmcnt(0)
	v_lshl_add_u64 v[36:37], v[6:7], 0, 0
	s_mov_b64 s[12:13], 0x1000
	v_lshl_add_u64 v[38:39], v[6:7], 0, s[12:13]
	s_mov_b64 s[12:13], 0x2000
	v_lshl_add_u64 v[40:41], v[6:7], 0, s[12:13]
	s_mov_b64 s[12:13], 0x3000
	v_lshl_add_u64 v[42:43], v[6:7], 0, s[12:13]
	global_load_dword v64, v[36:37], off
	global_load_dword v65, v[36:37], off offset:256
	global_load_dword v66, v[36:37], off offset:512
	global_load_dword v67, v[36:37], off offset:768
	global_load_dword v68, v[36:37], off offset:1024
	global_load_dword v69, v[36:37], off offset:1280
	global_load_dword v70, v[36:37], off offset:1536
	global_load_dword v71, v[36:37], off offset:1792
	global_load_dword v72, v[36:37], off offset:2048
	global_load_dword v73, v[36:37], off offset:2304
	global_load_dword v74, v[36:37], off offset:2560
	global_load_dword v75, v[36:37], off offset:2816
	global_load_dword v76, v[36:37], off offset:3072
	global_load_dword v77, v[36:37], off offset:3328
	global_load_dword v78, v[36:37], off offset:3584
	global_load_dword v79, v[36:37], off offset:3840
	global_load_dword v80, v[38:39], off
	global_load_dword v81, v[38:39], off offset:256
	global_load_dword v82, v[38:39], off offset:512
	global_load_dword v83, v[38:39], off offset:768
	global_load_dword v84, v[38:39], off offset:1024
	global_load_dword v85, v[38:39], off offset:1280
	global_load_dword v86, v[38:39], off offset:1536
	global_load_dword v87, v[38:39], off offset:1792
	global_load_dword v88, v[38:39], off offset:2048
	global_load_dword v89, v[38:39], off offset:2304
	global_load_dword v90, v[38:39], off offset:2560
	global_load_dword v91, v[38:39], off offset:2816
	global_load_dword v92, v[38:39], off offset:3072
	global_load_dword v93, v[38:39], off offset:3328
	global_load_dword v94, v[38:39], off offset:3584
	global_load_dword v95, v[38:39], off offset:3840
	global_load_dword v96, v[40:41], off
	global_load_dword v97, v[40:41], off offset:256
	global_load_dword v98, v[40:41], off offset:512
	global_load_dword v99, v[40:41], off offset:768
	global_load_dword v100, v[40:41], off offset:1024
	global_load_dword v101, v[40:41], off offset:1280
	global_load_dword v102, v[40:41], off offset:1536
	global_load_dword v103, v[40:41], off offset:1792
	global_load_dword v104, v[40:41], off offset:2048
	global_load_dword v105, v[40:41], off offset:2304
	global_load_dword v106, v[40:41], off offset:2560
	global_load_dword v107, v[40:41], off offset:2816
	global_load_dword v108, v[40:41], off offset:3072
	global_load_dword v109, v[40:41], off offset:3328
	global_load_dword v110, v[40:41], off offset:3584
	global_load_dword v111, v[40:41], off offset:3840
	global_load_dword v112, v[42:43], off
	global_load_dword v113, v[42:43], off offset:256
	global_load_dword v114, v[42:43], off offset:512
	global_load_dword v115, v[42:43], off offset:768
	global_load_dword v116, v[42:43], off offset:1024
	global_load_dword v117, v[42:43], off offset:1280
	global_load_dword v118, v[42:43], off offset:1536
	global_load_dword v119, v[42:43], off offset:1792
	v_and_b32_e32 v18, 56, v17
	v_lshl_add_u32 v18, v18, 2, v15
	ds_read_b32 v18, v18
	v_add_u32_e32 v19, v1, v17
	v_add_u32_e32 v28, v14, v17
	v_add_u32_e32 v29, v13, v17
	v_add_u32_e32 v30, v12, v17
	v_add_u32_e32 v31, v11, v17
	v_add_u32_e32 v32, v10, v17
	v_add_u32_e32 v33, v9, v17
	v_and_b32_e32 v19, 63, v19
	v_and_b32_e32 v28, 62, v28
	v_and_b32_e32 v29, 63, v29
	v_and_b32_e32 v30, 60, v30
	v_and_b32_e32 v31, 63, v31
	v_and_b32_e32 v32, 62, v32
	v_and_b32_e32 v33, 63, v33
	v_lshl_add_u32 v19, v19, 2, v15
	v_lshl_add_u32 v28, v28, 2, v15
	v_lshl_add_u32 v29, v29, 2, v15
	v_lshl_add_u32 v30, v30, 2, v15
	v_lshl_add_u32 v31, v31, 2, v15
	v_lshl_add_u32 v32, v32, 2, v15
	v_lshl_add_u32 v33, v33, 2, v15
	ds_read_b32 v19, v19
	ds_read_b32 v28, v28
	ds_read_b32 v29, v29
	ds_read_b32 v30, v30
	ds_read_b32 v31, v31
	ds_read_b32 v32, v32
	ds_read_b32 v33, v33
	v_add_u32_e32 v17, v17, v8
	s_waitcnt vmcnt(55) lgkmcnt(7)
	v_fmac_f32_e32 v16, v18, v64
	s_waitcnt vmcnt(54) lgkmcnt(6)
	v_fmac_f32_e32 v16, v19, v65
	s_waitcnt vmcnt(53) lgkmcnt(5)
	v_fmac_f32_e32 v16, v28, v66
	s_waitcnt vmcnt(52) lgkmcnt(4)
	v_fmac_f32_e32 v16, v29, v67
	s_waitcnt vmcnt(51) lgkmcnt(3)
	v_fmac_f32_e32 v16, v30, v68
	s_waitcnt vmcnt(50) lgkmcnt(2)
	v_fmac_f32_e32 v16, v31, v69
	s_waitcnt vmcnt(49) lgkmcnt(1)
	v_fmac_f32_e32 v16, v32, v70
	s_waitcnt vmcnt(48) lgkmcnt(0)
	v_fmac_f32_e32 v16, v33, v71
	global_load_dword v120, v[42:43], off offset:2048
	global_load_dword v121, v[42:43], off offset:2304
	global_load_dword v122, v[42:43], off offset:2560
	global_load_dword v123, v[42:43], off offset:2816
	global_load_dword v124, v[42:43], off offset:3072
	global_load_dword v125, v[42:43], off offset:3328
	global_load_dword v126, v[42:43], off offset:3584
	global_load_dword v127, v[42:43], off offset:3840
	v_and_b32_e32 v18, 56, v17
	v_lshl_add_u32 v18, v18, 2, v15
	ds_read_b32 v18, v18
	v_add_u32_e32 v19, v1, v17
	v_add_u32_e32 v28, v14, v17
	v_add_u32_e32 v29, v13, v17
	v_add_u32_e32 v30, v12, v17
	v_add_u32_e32 v31, v11, v17
	v_add_u32_e32 v32, v10, v17
	v_add_u32_e32 v33, v9, v17
	v_and_b32_e32 v19, 63, v19
	v_and_b32_e32 v28, 62, v28
	v_and_b32_e32 v29, 63, v29
	v_and_b32_e32 v30, 60, v30
	v_and_b32_e32 v31, 63, v31
	v_and_b32_e32 v32, 62, v32
	v_and_b32_e32 v33, 63, v33
	v_lshl_add_u32 v19, v19, 2, v15
	v_lshl_add_u32 v28, v28, 2, v15
	v_lshl_add_u32 v29, v29, 2, v15
	v_lshl_add_u32 v30, v30, 2, v15
	v_lshl_add_u32 v31, v31, 2, v15
	v_lshl_add_u32 v32, v32, 2, v15
	v_lshl_add_u32 v33, v33, 2, v15
	ds_read_b32 v19, v19
	ds_read_b32 v28, v28
	ds_read_b32 v29, v29
	ds_read_b32 v30, v30
	ds_read_b32 v31, v31
	ds_read_b32 v32, v32
	ds_read_b32 v33, v33
	v_add_u32_e32 v17, v17, v8
	s_waitcnt vmcnt(55) lgkmcnt(7)
; __device__ __forceinline__ void phase_p0a(const Ptrs& P, LAS unsigned char* lds, int tid_, int vcu, int G) {
;     ...
;     for (size_t i = gt; i < (size_t)NL * 2 * 4 * 64 * 64; i += NGT) { const int e = (int)(i & 63), d = (int)((i >> 6) & 63), h = (int)((i >> 12) & 3), kind = (int)((i >> 14) & 1), l = (int)(i >> 15);
;         const float* fw = P.four_w + ((size_t)(l * 4 + h) * 64) * 64 + e; float s = 0.f;
; #pragma unroll 8
;         for (int kp = 0; kp < 64; ++kp) s += t64[kind * 64 + ((kp * d) & 63)] * fw[kp * 64];
;         ((float*)(P.ws + WS_CSW))[i] = s * 0.00276213586f; }
	v_fmac_f32_e32 v16, v18, v72
	s_waitcnt vmcnt(54) lgkmcnt(6)
	v_fmac_f32_e32 v16, v19, v73
	s_waitcnt vmcnt(53) lgkmcnt(5)
	v_fmac_f32_e32 v16, v28, v74
	s_waitcnt vmcnt(52) lgkmcnt(4)
	v_fmac_f32_e32 v16, v29, v75
	s_waitcnt vmcnt(51) lgkmcnt(3)
	v_fmac_f32_e32 v16, v30, v76
	s_waitcnt vmcnt(50) lgkmcnt(2)
	v_fmac_f32_e32 v16, v31, v77
	s_waitcnt vmcnt(49) lgkmcnt(1)
	v_fmac_f32_e32 v16, v32, v78
	s_waitcnt vmcnt(48) lgkmcnt(0)
	v_fmac_f32_e32 v16, v33, v79
	v_and_b32_e32 v18, 56, v17
	v_lshl_add_u32 v18, v18, 2, v15
	ds_read_b32 v18, v18
	v_add_u32_e32 v19, v1, v17
	v_add_u32_e32 v28, v14, v17
	v_add_u32_e32 v29, v13, v17
	v_add_u32_e32 v30, v12, v17
	v_add_u32_e32 v31, v11, v17
	v_add_u32_e32 v32, v10, v17
	v_add_u32_e32 v33, v9, v17
	v_and_b32_e32 v19, 63, v19
	v_and_b32_e32 v28, 62, v28
	v_and_b32_e32 v29, 63, v29
	v_and_b32_e32 v30, 60, v30
	v_and_b32_e32 v31, 63, v31
	v_and_b32_e32 v32, 62, v32
	v_and_b32_e32 v33, 63, v33
	v_lshl_add_u32 v19, v19, 2, v15
	v_lshl_add_u32 v28, v28, 2, v15
	v_lshl_add_u32 v29, v29, 2, v15
	v_lshl_add_u32 v30, v30, 2, v15
	v_lshl_add_u32 v31, v31, 2, v15
	v_lshl_add_u32 v32, v32, 2, v15
	v_lshl_add_u32 v33, v33, 2, v15
	ds_read_b32 v19, v19
	ds_read_b32 v28, v28
	ds_read_b32 v29, v29
	ds_read_b32 v30, v30
	ds_read_b32 v31, v31
	ds_read_b32 v32, v32
	ds_read_b32 v33, v33
	v_add_u32_e32 v17, v17, v8
	s_waitcnt vmcnt(47) lgkmcnt(7)
	v_fmac_f32_e32 v16, v18, v80
	s_waitcnt vmcnt(46) lgkmcnt(6)
	v_fmac_f32_e32 v16, v19, v81
	s_waitcnt vmcnt(45) lgkmcnt(5)
	v_fmac_f32_e32 v16, v28, v82
	s_waitcnt vmcnt(44) lgkmcnt(4)
	v_fmac_f32_e32 v16, v29, v83
	s_waitcnt vmcnt(43) lgkmcnt(3)
	v_fmac_f32_e32 v16, v30, v84
	s_waitcnt vmcnt(42) lgkmcnt(2)
	v_fmac_f32_e32 v16, v31, v85
	s_waitcnt vmcnt(41) lgkmcnt(1)
	v_fmac_f32_e32 v16, v32, v86
	s_waitcnt vmcnt(40) lgkmcnt(0)
	v_fmac_f32_e32 v16, v33, v87
	v_and_b32_e32 v18, 56, v17
	v_lshl_add_u32 v18, v18, 2, v15
	ds_read_b32 v18, v18
	v_add_u32_e32 v19, v1, v17
	v_add_u32_e32 v28, v14, v17
	v_add_u32_e32 v29, v13, v17
	v_add_u32_e32 v30, v12, v17
	v_add_u32_e32 v31, v11, v17
	v_add_u32_e32 v32, v10, v17
	v_add_u32_e32 v33, v9, v17
	v_and_b32_e32 v19, 63, v19
	v_and_b32_e32 v28, 62, v28
	v_and_b32_e32 v29, 63, v29
	v_and_b32_e32 v30, 60, v30
	v_and_b32_e32 v31, 63, v31
	v_and_b32_e32 v32, 62, v32
	v_and_b32_e32 v33, 63, v33
	v_lshl_add_u32 v19, v19, 2, v15
	v_lshl_add_u32 v28, v28, 2, v15
	v_lshl_add_u32 v29, v29, 2, v15
	v_lshl_add_u32 v30, v30, 2, v15
	v_lshl_add_u32 v31, v31, 2, v15
	v_lshl_add_u32 v32, v32, 2, v15
	v_lshl_add_u32 v33, v33, 2, v15
	ds_read_b32 v19, v19
	ds_read_b32 v28, v28
	ds_read_b32 v29, v29
	ds_read_b32 v30, v30
	ds_read_b32 v31, v31
	ds_read_b32 v32, v32
	ds_read_b32 v33, v33
	v_add_u32_e32 v17, v17, v8
	s_waitcnt vmcnt(39) lgkmcnt(7)
	v_fmac_f32_e32 v16, v18, v88
	s_waitcnt vmcnt(38) lgkmcnt(6)
	v_fmac_f32_e32 v16, v19, v89
	s_waitcnt vmcnt(37) lgkmcnt(5)
	v_fmac_f32_e32 v16, v28, v90
	s_waitcnt vmcnt(36) lgkmcnt(4)
	v_fmac_f32_e32 v16, v29, v91
	s_waitcnt vmcnt(35) lgkmcnt(3)
	v_fmac_f32_e32 v16, v30, v92
	s_waitcnt vmcnt(34) lgkmcnt(2)
	v_fmac_f32_e32 v16, v31, v93
	s_waitcnt vmcnt(33) lgkmcnt(1)
	v_fmac_f32_e32 v16, v32, v94
	s_waitcnt vmcnt(32) lgkmcnt(0)
	v_fmac_f32_e32 v16, v33, v95
	v_and_b32_e32 v18, 56, v17
	v_lshl_add_u32 v18, v18, 2, v15
	ds_read_b32 v18, v18
	v_add_u32_e32 v19, v1, v17
	v_add_u32_e32 v28, v14, v17
	v_add_u32_e32 v29, v13, v17
	v_add_u32_e32 v30, v12, v17
	v_add_u32_e32 v31, v11, v17
	v_add_u32_e32 v32, v10, v17
	v_add_u32_e32 v33, v9, v17
	v_and_b32_e32 v19, 63, v19
	v_and_b32_e32 v28, 62, v28
	v_and_b32_e32 v29, 63, v29
	v_and_b32_e32 v30, 60, v30
	v_and_b32_e32 v31, 63, v31
	v_and_b32_e32 v32, 62, v32
	v_and_b32_e32 v33, 63, v33
	v_lshl_add_u32 v19, v19, 2, v15
	v_lshl_add_u32 v28, v28, 2, v15
	v_lshl_add_u32 v29, v29, 2, v15
	v_lshl_add_u32 v30, v30, 2, v15
	v_lshl_add_u32 v31, v31, 2, v15
	v_lshl_add_u32 v32, v32, 2, v15
	v_lshl_add_u32 v33, v33, 2, v15
	ds_read_b32 v19, v19
	ds_read_b32 v28, v28
	ds_read_b32 v29, v29
	ds_read_b32 v30, v30
	ds_read_b32 v31, v31
	ds_read_b32 v32, v32
	ds_read_b32 v33, v33
	v_add_u32_e32 v17, v17, v8
	s_waitcnt vmcnt(31) lgkmcnt(7)
	v_fmac_f32_e32 v16, v18, v96
	s_waitcnt vmcnt(30) lgkmcnt(6)
	v_fmac_f32_e32 v16, v19, v97
	s_waitcnt vmcnt(29) lgkmcnt(5)
	v_fmac_f32_e32 v16, v28, v98
	s_waitcnt vmcnt(28) lgkmcnt(4)
	v_fmac_f32_e32 v16, v29, v99
	s_waitcnt vmcnt(27) lgkmcnt(3)
	v_fmac_f32_e32 v16, v30, v100
	s_waitcnt vmcnt(26) lgkmcnt(2)
	v_fmac_f32_e32 v16, v31, v101
	s_waitcnt vmcnt(25) lgkmcnt(1)
; __device__ __forceinline__ void phase_p0a(const Ptrs& P, LAS unsigned char* lds, int tid_, int vcu, int G) {
;     ...
;     for (size_t i = gt; i < (size_t)NL * 2 * 4 * 64 * 64; i += NGT) { const int e = (int)(i & 63), d = (int)((i >> 6) & 63), h = (int)((i >> 12) & 3), kind = (int)((i >> 14) & 1), l = (int)(i >> 15);
;         const float* fw = P.four_w + ((size_t)(l * 4 + h) * 64) * 64 + e; float s = 0.f;
; #pragma unroll 8
;         for (int kp = 0; kp < 64; ++kp) s += t64[kind * 64 + ((kp * d) & 63)] * fw[kp * 64];
;         ((float*)(P.ws + WS_CSW))[i] = s * 0.00276213586f; }
	v_fmac_f32_e32 v16, v32, v102
	s_waitcnt vmcnt(24) lgkmcnt(0)
	v_fmac_f32_e32 v16, v33, v103
	v_and_b32_e32 v18, 56, v17
	v_lshl_add_u32 v18, v18, 2, v15
	ds_read_b32 v18, v18
	v_add_u32_e32 v19, v1, v17
	v_add_u32_e32 v28, v14, v17
	v_add_u32_e32 v29, v13, v17
	v_add_u32_e32 v30, v12, v17
	v_add_u32_e32 v31, v11, v17
	v_add_u32_e32 v32, v10, v17
	v_add_u32_e32 v33, v9, v17
	v_and_b32_e32 v19, 63, v19
	v_and_b32_e32 v28, 62, v28
	v_and_b32_e32 v29, 63, v29
	v_and_b32_e32 v30, 60, v30
	v_and_b32_e32 v31, 63, v31
	v_and_b32_e32 v32, 62, v32
	v_and_b32_e32 v33, 63, v33
	v_lshl_add_u32 v19, v19, 2, v15
	v_lshl_add_u32 v28, v28, 2, v15
	v_lshl_add_u32 v29, v29, 2, v15
	v_lshl_add_u32 v30, v30, 2, v15
	v_lshl_add_u32 v31, v31, 2, v15
	v_lshl_add_u32 v32, v32, 2, v15
	v_lshl_add_u32 v33, v33, 2, v15
	ds_read_b32 v19, v19
	ds_read_b32 v28, v28
	ds_read_b32 v29, v29
	ds_read_b32 v30, v30
	ds_read_b32 v31, v31
	ds_read_b32 v32, v32
	ds_read_b32 v33, v33
	v_add_u32_e32 v17, v17, v8
	s_waitcnt vmcnt(23) lgkmcnt(7)
	v_fmac_f32_e32 v16, v18, v104
	s_waitcnt vmcnt(22) lgkmcnt(6)
	v_fmac_f32_e32 v16, v19, v105
	s_waitcnt vmcnt(21) lgkmcnt(5)
	v_fmac_f32_e32 v16, v28, v106
	s_waitcnt vmcnt(20) lgkmcnt(4)
	v_fmac_f32_e32 v16, v29, v107
	s_waitcnt vmcnt(19) lgkmcnt(3)
	v_fmac_f32_e32 v16, v30, v108
	s_waitcnt vmcnt(18) lgkmcnt(2)
	v_fmac_f32_e32 v16, v31, v109
	s_waitcnt vmcnt(17) lgkmcnt(1)
	v_fmac_f32_e32 v16, v32, v110
	s_waitcnt vmcnt(16) lgkmcnt(0)
	v_fmac_f32_e32 v16, v33, v111
	v_and_b32_e32 v18, 56, v17
	v_lshl_add_u32 v18, v18, 2, v15
	ds_read_b32 v18, v18
	v_add_u32_e32 v19, v1, v17
	v_add_u32_e32 v28, v14, v17
	v_add_u32_e32 v29, v13, v17
	v_add_u32_e32 v30, v12, v17
	v_add_u32_e32 v31, v11, v17
	v_add_u32_e32 v32, v10, v17
	v_add_u32_e32 v33, v9, v17
	v_and_b32_e32 v19, 63, v19
	v_and_b32_e32 v28, 62, v28
	v_and_b32_e32 v29, 63, v29
	v_and_b32_e32 v30, 60, v30
	v_and_b32_e32 v31, 63, v31
	v_and_b32_e32 v32, 62, v32
	v_and_b32_e32 v33, 63, v33
	v_lshl_add_u32 v19, v19, 2, v15
	v_lshl_add_u32 v28, v28, 2, v15
	v_lshl_add_u32 v29, v29, 2, v15
	v_lshl_add_u32 v30, v30, 2, v15
	v_lshl_add_u32 v31, v31, 2, v15
	v_lshl_add_u32 v32, v32, 2, v15
	v_lshl_add_u32 v33, v33, 2, v15
	ds_read_b32 v19, v19
	ds_read_b32 v28, v28
	ds_read_b32 v29, v29
	ds_read_b32 v30, v30
	ds_read_b32 v31, v31
	ds_read_b32 v32, v32
	ds_read_b32 v33, v33
	v_add_u32_e32 v17, v17, v8
	s_waitcnt vmcnt(15) lgkmcnt(7)
	v_fmac_f32_e32 v16, v18, v112
	s_waitcnt vmcnt(14) lgkmcnt(6)
	v_fmac_f32_e32 v16, v19, v113
	s_waitcnt vmcnt(13) lgkmcnt(5)
	v_fmac_f32_e32 v16, v28, v114
	s_waitcnt vmcnt(12) lgkmcnt(4)
	v_fmac_f32_e32 v16, v29, v115
	s_waitcnt vmcnt(11) lgkmcnt(3)
	v_fmac_f32_e32 v16, v30, v116
	s_waitcnt vmcnt(10) lgkmcnt(2)
	v_fmac_f32_e32 v16, v31, v117
	s_waitcnt vmcnt(9) lgkmcnt(1)
	v_fmac_f32_e32 v16, v32, v118
	s_waitcnt vmcnt(8) lgkmcnt(0)
	v_fmac_f32_e32 v16, v33, v119
	v_and_b32_e32 v18, 56, v17
	v_lshl_add_u32 v18, v18, 2, v15
	ds_read_b32 v18, v18
	v_add_u32_e32 v19, v1, v17
	v_add_u32_e32 v28, v14, v17
	v_add_u32_e32 v29, v13, v17
	v_add_u32_e32 v30, v12, v17
	v_add_u32_e32 v31, v11, v17
	v_add_u32_e32 v32, v10, v17
	v_add_u32_e32 v33, v9, v17
	v_and_b32_e32 v19, 63, v19
	v_and_b32_e32 v28, 62, v28
	v_and_b32_e32 v29, 63, v29
	v_and_b32_e32 v30, 60, v30
	v_and_b32_e32 v31, 63, v31
	v_and_b32_e32 v32, 62, v32
	v_and_b32_e32 v33, 63, v33
	v_lshl_add_u32 v19, v19, 2, v15
	v_lshl_add_u32 v28, v28, 2, v15
	v_lshl_add_u32 v29, v29, 2, v15
	v_lshl_add_u32 v30, v30, 2, v15
	v_lshl_add_u32 v31, v31, 2, v15
	v_lshl_add_u32 v32, v32, 2, v15
	v_lshl_add_u32 v33, v33, 2, v15
	ds_read_b32 v19, v19
	ds_read_b32 v28, v28
	ds_read_b32 v29, v29
	ds_read_b32 v30, v30
	ds_read_b32 v31, v31
	ds_read_b32 v32, v32
	ds_read_b32 v33, v33
	v_add_u32_e32 v17, v17, v8
	s_waitcnt vmcnt(7) lgkmcnt(7)
	v_fmac_f32_e32 v16, v18, v120
	s_waitcnt vmcnt(6) lgkmcnt(6)
	v_fmac_f32_e32 v16, v19, v121
	s_waitcnt vmcnt(5) lgkmcnt(5)
	v_fmac_f32_e32 v16, v28, v122
	s_waitcnt vmcnt(4) lgkmcnt(4)
	v_fmac_f32_e32 v16, v29, v123
	s_waitcnt vmcnt(3) lgkmcnt(3)
	v_fmac_f32_e32 v16, v30, v124
	s_waitcnt vmcnt(2) lgkmcnt(2)
	v_fmac_f32_e32 v16, v31, v125
	s_waitcnt vmcnt(1) lgkmcnt(1)
	v_fmac_f32_e32 v16, v32, v126
	s_waitcnt vmcnt(0) lgkmcnt(0)
	v_fmac_f32_e32 v16, v33, v127
	v_lshl_add_u64 v[6:7], v[2:3], 2, s[0:1]
	v_lshl_add_u64 v[2:3], v[2:3], 0, s[6:7]
	v_cmp_lt_u64_e32 vcc, s[10:11], v[2:3]
	v_mul_f32_e32 v1, 0x3b3504f3, v16
	s_or_b64 s[8:9], vcc, s[8:9]
	global_store_dword v[6:7], v1, off
	s_andn2_b64 exec, exec, s[8:9]
	s_cbranch_execnz .LBB0_102

;     __device__ __forceinline__ void operator()(const f32x4 (&acc)[2][2][4][2], const Unit& u, int wr, int wc, int fr, int fq) const {
;         const int lane = fq * 16 + fr, frs = lane >> 2, fqs = lane & 3;
;         const int r0 = wr * 64 + frs, col0 = (u.pn & 3) * 256 + wc * 64 + 16 * fqs;
; #pragma unroll
;         for (int ai = 0; ai < 2; ++ai)
; #pragma unroll
;             for (int m = 0; m < 4; ++m) { const int r = r0 + ai * 128 + m * 16; const bool ok = r < u.aux1; const int pid = ok ? list[u.aux0 + r] : 0;
;                 v4u w;
;                 { const f32x4 a0 = acc[ai][0][m][0] * sc, a1 = acc[ai][0][m][1] * sc, a2 = acc[ai][1][m][0] * sc, a3 = acc[ai][1][m][1] * sc;
;                   w.x = (unsigned)__builtin_amdgcn_cvt_pk_fp8_f32(a0[2], a0[3], __builtin_amdgcn_cvt_pk_fp8_f32(a0[0], a0[1], 0, false), true);
;                   w.y = (unsigned)__builtin_amdgcn_cvt_pk_fp8_f32(a1[2], a1[3], __builtin_amdgcn_cvt_pk_fp8_f32(a1[0], a1[1], 0, false), true);
;                   w.z = (unsigned)__builtin_amdgcn_cvt_pk_fp8_f32(a2[2], a2[3], __builtin_amdgcn_cvt_pk_fp8_f32(a2[0], a2[1], 0, false), true);
;                   w.w = (unsigned)__builtin_amdgcn_cvt_pk_fp8_f32(a3[2], a3[3], __builtin_amdgcn_cvt_pk_fp8_f32(a3[0], a3[1], 0, false), true); }
;                 w = lane_xpose(w, lane);
;                 if (ok) *(v4u*)(Y + (size_t)pid * 1024 + col0) = w; }
.LBB0_1346:
	s_lshl_b32 s8, s8, 8
	s_and_b32 s8, s8, 0x300
	v_or_b32_e32 v162, s8, v143
	s_movk_i32 s63, 0x2440
	s_movk_i32 s62, 0x2000
	s_movk_i32 s61, 0xdff
	v_cmp_gt_i32_e32 vcc, s40, v137
	s_and_saveexec_b64 s[8:9], vcc
	v_lshl_add_u32 v170, s54, 2, v152
	ds_read_b32 v170, v170
	s_or_b64 exec, exec, s[8:9]
	v_cmp_gt_i32_e32 vcc, s40, v145
	s_and_saveexec_b64 s[8:9], vcc
	v_lshl_add_u32 v172, s54, 2, v153
	ds_read_b32 v172, v172
	s_or_b64 exec, exec, s[8:9]
	v_cmp_gt_i32_e32 vcc, s40, v146
	s_and_saveexec_b64 s[8:9], vcc
	v_lshl_add_u32 v174, s54, 2, v154
	ds_read_b32 v174, v174
	s_or_b64 exec, exec, s[8:9]
	v_cmp_gt_i32_e32 vcc, s40, v147
	s_and_saveexec_b64 s[8:9], vcc
	v_lshl_add_u32 v176, s54, 2, v155
	ds_read_b32 v176, v176
	s_or_b64 exec, exec, s[8:9]
	v_cmp_gt_i32_e32 vcc, s40, v148
	s_and_saveexec_b64 s[8:9], vcc
	v_lshl_add_u32 v178, s54, 2, v156
	ds_read_b32 v178, v178
	s_or_b64 exec, exec, s[8:9]
	v_cmp_gt_i32_e32 vcc, s40, v149
	s_and_saveexec_b64 s[8:9], vcc
	v_lshl_add_u32 v180, s54, 2, v157
	ds_read_b32 v180, v180
	s_or_b64 exec, exec, s[8:9]
	v_cmp_gt_i32_e32 vcc, s40, v150
	s_and_saveexec_b64 s[8:9], vcc
	v_lshl_add_u32 v182, s54, 2, v158
	ds_read_b32 v182, v182
	s_or_b64 exec, exec, s[8:9]
	v_cmp_gt_i32_e32 vcc, s40, v151
	s_and_saveexec_b64 s[8:9], vcc
	v_lshl_add_u32 v184, s54, 2, v159
	ds_read_b32 v184, v184
	s_or_b64 exec, exec, s[8:9]
	v_cvt_pk_fp8_f32 v200, v114, v115
	v_cvt_pk_fp8_f32 v201, v118, v119
	v_cvt_pk_fp8_f32 v202, v122, v123
	v_cvt_pk_fp8_f32 v203, v126, v127
	v_cvt_pk_fp8_f32 v200, v116, v117 op_sel:[0,0,1]
	v_cvt_pk_fp8_f32 v201, v120, v121 op_sel:[0,0,1]
	v_cvt_pk_fp8_f32 v202, v124, v125 op_sel:[0,0,1]
	v_cvt_pk_fp8_f32 v203, v128, v129 op_sel:[0,0,1]
	s_nop 0
	ds_bpermute_b32 v114, v144, v200
	ds_bpermute_b32 v115, v144, v201
	ds_bpermute_b32 v116, v144, v202
	ds_bpermute_b32 v117, v144, v203
	v_cvt_pk_fp8_f32 v204, v102, v103
	v_cvt_pk_fp8_f32 v205, v98, v99
	v_cvt_pk_fp8_f32 v206, v110, v111
	v_cvt_pk_fp8_f32 v207, v106, v107
	v_cvt_pk_fp8_f32 v204, v104, v105 op_sel:[0,0,1]
	v_cvt_pk_fp8_f32 v205, v100, v101 op_sel:[0,0,1]
	v_cvt_pk_fp8_f32 v206, v112, v113 op_sel:[0,0,1]
	v_cvt_pk_fp8_f32 v207, v108, v109 op_sel:[0,0,1]
	s_nop 0
	ds_bpermute_b32 v102, v144, v204
	ds_bpermute_b32 v103, v144, v205
	ds_bpermute_b32 v104, v144, v206
	ds_bpermute_b32 v105, v144, v207
	s_waitcnt lgkmcnt(4)
	v_ashrrev_i32_e32 v171, 31, v170
	v_lshlrev_b64 v[170:171], 10, v[170:171]
	v_lshl_add_u64 v[170:171], s[12:13], 0, v[170:171]
	v_lshl_add_u64 v[170:171], v[170:171], 0, v[162:163]
	v_cmp_gt_i32_e32 vcc, s40, v137
	s_and_saveexec_b64 s[8:9], vcc
	global_store_dwordx4 v[170:171], v[114:117], off
	s_or_b64 exec, exec, s[8:9]
	v_cvt_pk_fp8_f32 v208, v86, v87
	v_cvt_pk_fp8_f32 v209, v82, v83
	v_cvt_pk_fp8_f32 v210, v94, v95
	v_cvt_pk_fp8_f32 v211, v90, v91
	v_cvt_pk_fp8_f32 v208, v88, v89 op_sel:[0,0,1]
	v_cvt_pk_fp8_f32 v209, v84, v85 op_sel:[0,0,1]
	v_cvt_pk_fp8_f32 v210, v96, v97 op_sel:[0,0,1]
	v_cvt_pk_fp8_f32 v211, v92, v93 op_sel:[0,0,1]
	s_nop 0
	ds_bpermute_b32 v86, v144, v208
	ds_bpermute_b32 v87, v144, v209
	ds_bpermute_b32 v88, v144, v210
	ds_bpermute_b32 v89, v144, v211
	s_waitcnt lgkmcnt(4)
	v_ashrrev_i32_e32 v173, 31, v172
	v_lshlrev_b64 v[172:173], 10, v[172:173]
	v_lshl_add_u64 v[172:173], s[12:13], 0, v[172:173]
	v_lshl_add_u64 v[172:173], v[172:173], 0, v[162:163]
	v_cmp_gt_i32_e32 vcc, s40, v145
	s_and_saveexec_b64 s[8:9], vcc
	global_store_dwordx4 v[172:173], v[102:105], off
	s_or_b64 exec, exec, s[8:9]
	v_cvt_pk_fp8_f32 v212, v54, v55
	v_cvt_pk_fp8_f32 v213, v50, v51
	v_cvt_pk_fp8_f32 v214, v70, v71
	v_cvt_pk_fp8_f32 v215, v66, v67
	v_cvt_pk_fp8_f32 v212, v56, v57 op_sel:[0,0,1]
	v_cvt_pk_fp8_f32 v213, v52, v53 op_sel:[0,0,1]
	v_cvt_pk_fp8_f32 v214, v72, v73 op_sel:[0,0,1]
	v_cvt_pk_fp8_f32 v215, v68, v69 op_sel:[0,0,1]
	s_nop 0
	ds_bpermute_b32 v54, v144, v212
	ds_bpermute_b32 v55, v144, v213
	ds_bpermute_b32 v56, v144, v214
	ds_bpermute_b32 v57, v144, v215
	s_waitcnt lgkmcnt(4)
;     __device__ __forceinline__ void operator()(const f32x4 (&acc)[2][2][4][2], const Unit& u, int wr, int wc, int fr, int fq) const {
;     ...
;             for (int m = 0; m < 4; ++m) { const int r = r0 + ai * 128 + m * 16; const bool ok = r < u.aux1; const int pid = ok ? list[u.aux0 + r] : 0;
;                 v4u w;
;                 { const f32x4 a0 = acc[ai][0][m][0] * sc, a1 = acc[ai][0][m][1] * sc, a2 = acc[ai][1][m][0] * sc, a3 = acc[ai][1][m][1] * sc;
;                   w.x = (unsigned)__builtin_amdgcn_cvt_pk_fp8_f32(a0[2], a0[3], __builtin_amdgcn_cvt_pk_fp8_f32(a0[0], a0[1], 0, false), true);
;                   w.y = (unsigned)__builtin_amdgcn_cvt_pk_fp8_f32(a1[2], a1[3], __builtin_amdgcn_cvt_pk_fp8_f32(a1[0], a1[1], 0, false), true);
;                   w.z = (unsigned)__builtin_amdgcn_cvt_pk_fp8_f32(a2[2], a2[3], __builtin_amdgcn_cvt_pk_fp8_f32(a2[0], a2[1], 0, false), true);
;                   w.w = (unsigned)__builtin_amdgcn_cvt_pk_fp8_f32(a3[2], a3[3], __builtin_amdgcn_cvt_pk_fp8_f32(a3[0], a3[1], 0, false), true); }
;                 w = lane_xpose(w, lane);
;                 if (ok) *(v4u*)(Y + (size_t)pid * 1024 + col0) = w; }
	v_ashrrev_i32_e32 v175, 31, v174
	v_lshlrev_b64 v[174:175], 10, v[174:175]
	v_lshl_add_u64 v[174:175], s[12:13], 0, v[174:175]
	v_lshl_add_u64 v[174:175], v[174:175], 0, v[162:163]
	v_cmp_gt_i32_e32 vcc, s40, v146
	s_and_saveexec_b64 s[8:9], vcc
	global_store_dwordx4 v[174:175], v[86:89], off
	s_or_b64 exec, exec, s[8:9]
	v_cvt_pk_fp8_f32 v216, v62, v63
	v_cvt_pk_fp8_f32 v217, v58, v59
	v_cvt_pk_fp8_f32 v218, v78, v79
	v_cvt_pk_fp8_f32 v219, v74, v75
	v_cvt_pk_fp8_f32 v216, v64, v65 op_sel:[0,0,1]
	v_cvt_pk_fp8_f32 v217, v60, v61 op_sel:[0,0,1]
	v_cvt_pk_fp8_f32 v218, v80, v81 op_sel:[0,0,1]
	v_cvt_pk_fp8_f32 v219, v76, v77 op_sel:[0,0,1]
	s_nop 0
	ds_bpermute_b32 v62, v144, v216
	ds_bpermute_b32 v63, v144, v217
	ds_bpermute_b32 v64, v144, v218
	ds_bpermute_b32 v65, v144, v219
	s_waitcnt lgkmcnt(4)
	v_ashrrev_i32_e32 v177, 31, v176
	v_lshlrev_b64 v[176:177], 10, v[176:177]
	v_lshl_add_u64 v[176:177], s[12:13], 0, v[176:177]
	v_lshl_add_u64 v[176:177], v[176:177], 0, v[162:163]
	v_cmp_gt_i32_e32 vcc, s40, v147
	s_and_saveexec_b64 s[8:9], vcc
	global_store_dwordx4 v[176:177], v[54:57], off
	s_or_b64 exec, exec, s[8:9]
	v_cvt_pk_fp8_f32 v220, v38, v39
	v_cvt_pk_fp8_f32 v221, v34, v35
	v_cvt_pk_fp8_f32 v222, v46, v47
	v_cvt_pk_fp8_f32 v223, v42, v43
	v_cvt_pk_fp8_f32 v220, v40, v41 op_sel:[0,0,1]
	v_cvt_pk_fp8_f32 v221, v36, v37 op_sel:[0,0,1]
	v_cvt_pk_fp8_f32 v222, v48, v49 op_sel:[0,0,1]
	v_cvt_pk_fp8_f32 v223, v44, v45 op_sel:[0,0,1]
	s_nop 0
	ds_bpermute_b32 v38, v144, v220
	ds_bpermute_b32 v39, v144, v221
	ds_bpermute_b32 v40, v144, v222
	ds_bpermute_b32 v41, v144, v223
	s_waitcnt lgkmcnt(4)
	v_ashrrev_i32_e32 v179, 31, v178
	v_lshlrev_b64 v[178:179], 10, v[178:179]
	v_lshl_add_u64 v[178:179], s[12:13], 0, v[178:179]
	v_lshl_add_u64 v[178:179], v[178:179], 0, v[162:163]
	v_cmp_gt_i32_e32 vcc, s40, v148
	s_and_saveexec_b64 s[8:9], vcc
	global_store_dwordx4 v[178:179], v[62:65], off
	s_or_b64 exec, exec, s[8:9]
	v_cvt_pk_fp8_f32 v224, v22, v23
	v_cvt_pk_fp8_f32 v225, v18, v19
	v_cvt_pk_fp8_f32 v226, v30, v31
	v_cvt_pk_fp8_f32 v227, v26, v27
	v_cvt_pk_fp8_f32 v224, v24, v25 op_sel:[0,0,1]
	v_cvt_pk_fp8_f32 v225, v20, v21 op_sel:[0,0,1]
	v_cvt_pk_fp8_f32 v226, v32, v33 op_sel:[0,0,1]
	v_cvt_pk_fp8_f32 v227, v28, v29 op_sel:[0,0,1]
	s_nop 0
	ds_bpermute_b32 v22, v144, v224
	ds_bpermute_b32 v23, v144, v225
	ds_bpermute_b32 v24, v144, v226
	ds_bpermute_b32 v25, v144, v227
	s_waitcnt lgkmcnt(4)
	v_ashrrev_i32_e32 v181, 31, v180
	v_lshlrev_b64 v[180:181], 10, v[180:181]
	v_lshl_add_u64 v[180:181], s[12:13], 0, v[180:181]
	v_lshl_add_u64 v[180:181], v[180:181], 0, v[162:163]
	v_cmp_gt_i32_e32 vcc, s40, v149
	s_and_saveexec_b64 s[8:9], vcc
	global_store_dwordx4 v[180:181], v[38:41], off
	s_or_b64 exec, exec, s[8:9]
	v_cvt_pk_fp8_f32 v228, v10, v11
	v_cvt_pk_fp8_f32 v229, v6, v7
	v_cvt_pk_fp8_f32 v230, v14, v15
	v_cvt_pk_fp8_f32 v231, v2, v3
	v_cvt_pk_fp8_f32 v228, v12, v13 op_sel:[0,0,1]
	v_cvt_pk_fp8_f32 v229, v8, v9 op_sel:[0,0,1]
	v_cvt_pk_fp8_f32 v230, v16, v17 op_sel:[0,0,1]
	v_cvt_pk_fp8_f32 v231, v4, v5 op_sel:[0,0,1]
	s_nop 0
	ds_bpermute_b32 v10, v144, v228
	ds_bpermute_b32 v11, v144, v229
	ds_bpermute_b32 v12, v144, v230
	ds_bpermute_b32 v13, v144, v231
	s_waitcnt lgkmcnt(4)
	v_ashrrev_i32_e32 v183, 31, v182
	v_lshlrev_b64 v[182:183], 10, v[182:183]
	v_lshl_add_u64 v[182:183], s[12:13], 0, v[182:183]
	v_lshl_add_u64 v[182:183], v[182:183], 0, v[162:163]
	v_cmp_gt_i32_e32 vcc, s40, v150
	s_and_saveexec_b64 s[8:9], vcc
	global_store_dwordx4 v[182:183], v[22:25], off
	s_or_b64 exec, exec, s[8:9]
	s_waitcnt lgkmcnt(0)
	v_ashrrev_i32_e32 v185, 31, v184
	v_lshlrev_b64 v[184:185], 10, v[184:185]
	v_lshl_add_u64 v[184:185], s[12:13], 0, v[184:185]
	v_lshl_add_u64 v[184:185], v[184:185], 0, v[162:163]
	v_cmp_gt_i32_e32 vcc, s40, v151
	s_and_saveexec_b64 s[8:9], vcc
	global_store_dwordx4 v[184:185], v[10:13], off
	s_or_b64 exec, exec, s[8:9]
	s_cmp_eq_u32 s4, s48
	s_mov_b64 s[8:9], -1
	s_cbranch_scc1 .LBB0_1339
	s_andn2_b64 vcc, exec, s[6:7]
	s_cbranch_vccnz .LBB0_1338
	s_barrier
	s_branch .LBB0_1338
